# indexer: next-unit ticket atomic no longer waited for at the unit head (returns into a spare VGPR, consumed after the scoring loop); on top of DSA table mask + trims
# baseline (speedup 1.0000x reference)
.LBB0_1231:
	s_waitcnt lgkmcnt(1)
	v_mov_b32_e32 v0, 0
	s_and_saveexec_b64 s[40:41], s[36:37]
	s_cbranch_execz .LBB0_1235
	s_mov_b64 s[44:45], exec
	v_mbcnt_lo_u32_b32 v0, s44, 0
	v_mbcnt_hi_u32_b32 v0, s45, v0
	v_cmp_eq_u32_e32 vcc, 0, v0
	s_and_saveexec_b64 s[42:43], vcc
	s_cbranch_execz .LBB0_1234
	s_bcnt1_i32_b64 s0, s[44:45]
	s_waitcnt lgkmcnt(0)
	v_mov_b32_e32 v2, s0
	v_readlane_b32 s0, v253, 53
	v_readlane_b32 s1, v253, 54
	s_nop 4
	global_atomic_add v229, v1, v2, s[0:1] sc0
.LBB0_1234:
	s_or_b64 exec, exec, s[42:43]
.LBB0_1235:
	s_or_b64 exec, exec, s[40:41]
	s_not_b32 s1, s17
	s_lshl_b32 s1, s1, 1
	s_and_b32 s0, s17, 1
	s_and_b32 s34, s1, 0x1ffc
	s_bfe_u32 s1, s1, 0x80005
	v_readlane_b32 s40, v253, 32
	s_cmp_gt_i32 s40, s1
	v_readlane_b32 s41, v253, 33
	s_cbranch_scc1 .LBB0_1248
	v_or_b32_e32 v108, s34, v140
	s_lshl_b32 s17, s0, 8
	v_or_b32_e32 v109, 2, v108
	v_mov_b32_e32 v110, v148
	v_mov_b32_e32 v111, v147
	v_readlane_b32 s29, v253, 52
	s_branch .LBB0_1238

.LBB0_1248:
	s_and_saveexec_b64 s[40:41], s[84:85]
	ds_write_b32 v142, v1
	s_or_b64 exec, exec, s[40:41]
	s_andn2_b32 s17, 1, s35
	s_and_saveexec_b64 s[40:41], s[36:37]
	s_cbranch_execz .LBB0_1252
	s_lshl_b32 s29, s17, 2
	s_or_b32 s29, s29, 0x20420
	s_waitcnt lgkmcnt(0)
	v_mov_b32_e32 v2, s29
	s_waitcnt vmcnt(0)
	v_add_u32_e32 v0, v229, v0
	ds_write_b32 v2, v0
